# c4
# baseline (speedup 1.0000x reference)
.LBB6_525:
	s_or_b64 exec, exec, s[10:11]
	v_mov_b32_e32 v33, v24
	v_mov_b32_e32 v24, v25
	v_mov_b32_e32 v25, v26
	v_pk_add_f32 v[184:185], v[68:69], v[24:25]
	v_mov_b32_e32 v24, v82
	v_mov_b32_e32 v25, v70
	v_mov_b32_e32 v26, v55
	v_pk_add_f32 v[180:181], v[24:25], v[26:27]
	v_mov_b32_e32 v24, v83
	v_mov_b32_e32 v25, v84
	v_mov_b32_e32 v32, v23
	v_pk_add_f32 v[186:187], v[24:25], v[56:57]
	v_mov_b32_e32 v24, v85
	v_mov_b32_e32 v25, v86
	v_pk_add_f32 v[182:183], v[66:67], v[32:33]
	v_pk_add_f32 v[188:189], v[24:25], v[58:59]
	s_waitcnt lgkmcnt(1)
	v_mfma_f32_32x32x16_f16 v[2:17], v[116:119], v[60:63], v[2:17]
	s_waitcnt lgkmcnt(0)
	v_mfma_f32_32x32x16_f16 v[2:17], v[112:115], v[28:31], v[2:17]
	s_add_i32 s3, s3, s33
	s_bfe_u32 s3, s3, 0x30003
	s_lshl_b32 s10, s3, 17
	s_lshl_b32 s2, s2, 9
	s_add_i32 s10, s40, s10
	s_and_b32 s2, s2, 0x7000
	s_add_i32 s2, s2, s10
	s_nop 4
	v_lshl_add_u32 v17, v200, 15, s2
	v_add_lshl_u32 v23, v201, v191, 10
	s_movk_i32 s10, 0xfc80
	v_add3_u32 v193, v17, v23, s10
	v_lshl_add_u32 v17, v198, 15, s2
	v_add_lshl_u32 v23, v199, v197, 10
	s_mov_b32 s10, 0xffff7c80
	v_add3_u32 v216, v17, v23, s10
	v_lshl_add_u32 v17, v195, 15, s2
	v_add_lshl_u32 v23, v196, v191, 10
	v_add3_u32 v217, v17, v23, s10
	s_lshl_b32 s2, s3, 7
	v_lshlrev_b32_e32 v17, 5, v194
	v_or3_b32 v17, v190, s2, v17
	v_add_u32_e32 v17, s41, v17
	v_add_lshl_u32 v17, v17, v202, 10
	v_add3_u32 v32, s40, v17, v206
	v_mov_b32_e32 v33, 0
	v_add_u32_e32 v17, 32, v32
	v_lshlrev_b64 v[194:195], 4, v[32:33]
	v_lshl_add_u64 v[24:25], v[32:33], 2, s[18:19]
	s_mov_b64 s[10:11], 0x100
	v_lshlrev_b32_e32 v32, 2, v17
	s_mov_b32 s33, 2
	v_lshl_add_u64 v[196:197], v[24:25], 0, s[10:11]
	v_lshl_add_u64 v[198:199], s[18:19], 0, v[32:33]
	v_lshlrev_b32_e32 v200, 4, v17
	v_mov_b32_e32 v201, v33
	v_mov_b32_e32 v230, 0
	v_mov_b32_e32 v231, 0
	v_mov_b32_e32 v232, 0
	v_mov_b32_e32 v233, 0
	v_mov_b32_e32 v234, 0
	v_mov_b32_e32 v235, 0
	v_mov_b32_e32 v236, 0
	v_mov_b32_e32 v237, 0
	v_mov_b32_e32 v238, 0
	v_mov_b32_e32 v239, 0
	s_barrier
.LBB6_526:
	ds_read_b128 v[24:27], v209
	ds_read_b128 v[72:75], v209 offset:1056
	ds_read_b128 v[28:31], v211
	ds_read_b128 v[96:99], v209 offset:2112
	ds_read_b128 v[100:103], v211 offset:1056
	ds_read_b128 v[92:95], v211 offset:2112
	s_add_i32 s33, s33, 2
	v_or_b32_e32 v17, s33, v1
	s_waitcnt lgkmcnt(5)
	v_mfma_f32_32x32x16_f16 v[56:71], v[176:179], v[24:27], 0
	v_cmp_gt_u32_e64 s[2:3], 32, v17
	s_and_b64 s[28:29], vcc, s[2:3]
	v_add_u32_e32 v32, v206, v217
	s_waitcnt lgkmcnt(3)
	v_mfma_f32_32x32x16_f16 v[56:71], v[172:175], v[28:31], v[56:71]
	s_and_saveexec_b64 s[2:3], s[28:29]
	s_cbranch_execz .LBB6_528
	v_lshl_add_u64 v[24:25], v[32:33], 4, s[12:13]
	global_load_dwordx4 v[232:235], v[24:25], off
	v_lshl_add_u64 v[24:25], v[32:33], 2, s[14:15]
	global_load_dword v230, v[24:25], off
.LBB6_528:
	s_or_b64 exec, exec, s[2:3]
	v_or_b32_e32 v17, s33, v208
	v_cmp_gt_u32_e64 s[2:3], 32, v17
	s_and_b64 s[30:31], s[22:23], s[2:3]
	v_mov_b32_e32 v17, 0
	v_add_u32_e32 v202, v206, v216
	s_and_saveexec_b64 s[2:3], s[30:31]
	s_cbranch_execz .LBB6_530
	v_mov_b32_e32 v203, v33
	v_lshl_add_u64 v[24:25], v[202:203], 4, s[12:13]
	global_load_dwordx4 v[236:239], v[24:25], off
	v_lshl_add_u64 v[24:25], v[202:203], 2, s[14:15]
	global_load_dword v231, v[24:25], off

.LBB6_532:
	s_or_b64 exec, exec, s[34:35]
	v_mfma_f32_32x32x16_f16 v[56:71], v[164:167], v[72:75], v[56:71]
	ds_read_b128 v[218:221], v209 offset:3168
	ds_read_b128 v[222:225], v211 offset:3168
	v_mfma_f32_32x32x16_f16 v[72:87], v[176:179], v[72:75], 0
	s_waitcnt lgkmcnt(3)
	v_mfma_f32_32x32x16_f16 v[56:71], v[160:163], v[100:103], v[56:71]
	v_mfma_f32_32x32x16_f16 v[72:87], v[172:175], v[100:103], v[72:87]
	v_mfma_f32_32x32x16_f16 v[56:71], v[168:171], v[96:99], v[56:71]
	v_mfma_f32_32x32x16_f16 v[72:87], v[164:167], v[96:99], v[72:87]
	ds_read_b128 v[96:99], v209 offset:6336
	ds_read_b128 v[100:103], v211 offset:6336
	s_waitcnt lgkmcnt(4)
	v_mfma_f32_32x32x16_f16 v[56:71], v[156:159], v[92:95], v[56:71]
	v_mfma_f32_32x32x16_f16 v[72:87], v[160:163], v[92:95], v[72:87]
	v_add_f32_e32 v14, v187, v14
	v_add_f32_e32 v15, v188, v15
	s_waitcnt lgkmcnt(3)
	v_mfma_f32_32x32x16_f16 v[72:87], v[168:171], v[218:221], v[72:87]
	v_add_f32_e32 v12, v180, v12
	v_add_f32_e32 v13, v186, v13
	v_max_f32_e32 v14, 0, v14
	v_max_f32_e32 v15, 0, v15
	v_max_f32_e32 v12, 0, v12
	v_max_f32_e32 v13, 0, v13
	v_cvt_pk_f16_f32 v15, v14, v15
	v_cvt_pk_f16_f32 v14, v12, v13
	v_add_f32_e32 v12, v189, v16
	v_max_f32_e32 v16, 0, v12
	v_add_f32_e32 v12, v184, v46
	v_add_f32_e32 v13, v185, v47
	v_max_f32_e32 v12, 0, v12
	v_max_f32_e32 v13, 0, v13
	s_waitcnt lgkmcnt(2)
	v_mfma_f32_32x32x16_f16 v[72:87], v[156:159], v[222:225], v[72:87]
	v_cvt_pk_f16_f32 v13, v12, v13
	v_add_f32_e32 v12, v182, v44
	v_add_f32_e32 v44, v183, v45
	v_max_f32_e32 v12, 0, v12
	v_max_f32_e32 v44, 0, v44
	ds_read_b128 v[92:95], v209 offset:7392
	ds_read_b128 v[226:229], v211 offset:7392
	v_cvt_pk_f16_f32 v12, v12, v44
	v_add_f32_e32 v44, v181, v48
	v_max_f32_e32 v46, 0, v44
	v_permlane32_swap_b32_e32 v12, v14
	v_permlane32_swap_b32_e32 v13, v15
	v_permlane32_swap_b32_e32 v46, v16
	v_lshl_add_u64 v[44:45], s[20:21], 0, v[200:201]
	global_store_dwordx4 v[44:45], v[12:15], off sc1
	s_nop 1
	v_cvt_pk_f16_f32 v12, v46, v16
	global_store_dword v[198:199], v12, off sc1
	s_waitcnt lgkmcnt(3)
	v_mfma_f32_32x32x16_f16 v[56:71], v[132:135], v[96:99], v[56:71]
	ds_read_b128 v[96:99], v209 offset:8448
	ds_read_b128 v[180:183], v211 offset:8448
	s_waitcnt lgkmcnt(4)
	v_mfma_f32_32x32x16_f16 v[56:71], v[140:143], v[100:103], v[56:71]
	s_waitcnt lgkmcnt(3)
	v_mfma_f32_32x32x16_f16 v[56:71], v[120:123], v[92:95], v[56:71]
	ds_read_b128 v[12:15], v209 offset:9504
	ds_read_b128 v[44:47], v211 offset:9504
	v_mfma_f32_32x32x16_f16 v[72:87], v[132:135], v[92:95], v[72:87]
	s_waitcnt lgkmcnt(4)
	v_mfma_f32_32x32x16_f16 v[56:71], v[152:155], v[226:229], v[56:71]
	v_mfma_f32_32x32x16_f16 v[72:87], v[140:143], v[226:229], v[72:87]
	s_waitcnt lgkmcnt(3)
	v_mfma_f32_32x32x16_f16 v[56:71], v[148:151], v[96:99], v[56:71]
	s_mov_b64 s[34:35], s[26:27]
	v_mfma_f32_32x32x16_f16 v[72:87], v[120:123], v[96:99], v[72:87]
	ds_read_b128 v[100:103], v209 offset:12672
	ds_read_b128 v[96:99], v211 offset:12672
	s_waitcnt vmcnt(3)
	ds_write_b128 v212, v[232:235] offset:38032
	s_waitcnt vmcnt(2)
	ds_write_b32 v212, v230 offset:38564
	s_waitcnt lgkmcnt(6)
	v_mfma_f32_32x32x16_f16 v[56:71], v[144:147], v[180:183], v[56:71]
	v_mfma_f32_32x32x16_f16 v[72:87], v[152:155], v[180:183], v[72:87]
	s_and_saveexec_b64 s[36:37], s[4:5]
	s_andn2_b64 s[34:35], s[26:27], exec
	s_and_b64 s[38:39], s[6:7], exec
	s_or_b64 s[34:35], s[34:35], s[38:39]
	ds_write_b32 v212, v230 offset:38552
	s_or_b64 exec, exec, s[36:37]
	s_and_saveexec_b64 s[36:37], s[34:35]
	ds_write_b32 v212, v230 offset:38576
	s_or_b64 exec, exec, s[36:37]
	s_waitcnt lgkmcnt(5)
	v_mfma_f32_32x32x16_f16 v[72:87], v[148:151], v[12:15], v[72:87]
	ds_read_b128 v[92:95], v209 offset:13728
	ds_read_b128 v[12:15], v211 offset:13728
	s_waitcnt lgkmcnt(6)
	v_mfma_f32_32x32x16_f16 v[72:87], v[144:147], v[44:47], v[72:87]
	s_waitcnt lgkmcnt(5)
	v_mfma_f32_32x32x16_f16 v[56:71], v[136:139], v[100:103], v[56:71]
	ds_read_b128 v[88:91], v209 offset:14784
	ds_read_b128 v[44:47], v211 offset:14784
	s_waitcnt lgkmcnt(6)
	v_mfma_f32_32x32x16_f16 v[56:71], v[108:111], v[96:99], v[56:71]
	s_and_saveexec_b64 s[34:35], s[0:1]
	s_cbranch_execz .LBB6_541
	s_mov_b64 s[38:39], s[26:27]
	ds_write_b128 v214, v[236:239] offset:38032
	ds_write_b32 v214, v231 offset:38564
	s_and_saveexec_b64 s[36:37], s[4:5]
	s_andn2_b64 s[38:39], s[26:27], exec
	s_and_b64 s[42:43], s[6:7], exec
	s_or_b64 s[38:39], s[38:39], s[42:43]
	ds_write_b32 v214, v231 offset:38552
	s_or_b64 exec, exec, s[36:37]
	s_and_b64 exec, exec, s[38:39]
	ds_write_b32 v214, v231 offset:38576

.LBB6_546:
	s_or_b64 exec, exec, s[34:35]
	s_waitcnt lgkmcnt(0)
	s_barrier
	ds_read_b128 v[24:27], v209 offset:38016
	ds_read_b128 v[12:15], v209 offset:39072
	v_mfma_f32_32x32x16_f16 v[56:71], v[116:119], v[88:91], v[56:71]
	v_mfma_f32_32x32x16_f16 v[72:87], v[128:131], v[88:91], v[72:87]
	v_mfma_f32_32x32x16_f16 v[56:71], v[112:115], v[44:47], v[56:71]
	v_mfma_f32_32x32x16_f16 v[72:87], v[124:127], v[44:47], v[72:87]
	v_mfma_f32_32x32x16_f16 v[72:87], v[116:119], v[92:95], v[72:87]
	v_mfma_f32_32x32x16_f16 v[72:87], v[112:115], v[28:31], v[72:87]
	s_waitcnt lgkmcnt(1)
	v_mfma_f32_32x32x16_f16 v[88:103], v[176:179], v[24:27], 0
	ds_read_b128 v[24:27], v211 offset:38016
	ds_read_b128 v[184:187], v209 offset:40128
	ds_read_b128 v[188:191], v211 offset:39072
	ds_read_b128 v[180:183], v211 offset:40128
	s_nop 1
	s_waitcnt lgkmcnt(3)
	v_mfma_f32_32x32x16_f16 v[88:103], v[172:175], v[24:27], v[88:103]
	s_and_saveexec_b64 s[34:35], s[28:29]
	s_cbranch_execz .LBB6_548
	v_lshl_add_u64 v[16:17], v[32:33], 4, s[12:13]
	global_load_dwordx4 v[232:235], v[16:17], off offset:512
	v_lshl_add_u64 v[16:17], v[32:33], 2, s[14:15]
	global_load_dword v230, v[16:17], off offset:128
.LBB6_548:
	s_or_b64 exec, exec, s[34:35]
	s_and_saveexec_b64 s[28:29], s[30:31]
	s_cbranch_execz .LBB6_550
	v_mov_b32_e32 v203, v33
	v_lshl_add_u64 v[16:17], v[202:203], 4, s[12:13]
	global_load_dwordx4 v[236:239], v[16:17], off offset:512
	v_lshl_add_u64 v[16:17], v[202:203], 2, s[14:15]
	global_load_dword v231, v[16:17], off offset:128

.LBB6_552:
	s_or_b64 exec, exec, s[28:29]
	v_add_f32_e32 v39, v18, v39
	v_add_f32_e32 v202, v19, v40
	v_add_f32_e32 v203, v20, v41
	v_add_f32_e32 v204, v21, v42
	v_add_f32_e32 v205, v22, v43
	v_add_f32_e32 v7, v50, v7
	v_add_f32_e32 v218, v51, v8
	v_add_f32_e32 v219, v52, v9
	v_add_f32_e32 v220, v53, v10
	v_add_f32_e32 v221, v54, v11
	v_mfma_f32_32x32x16_f16 v[88:103], v[164:167], v[12:15], v[88:103]
	ds_read_b128 v[40:43], v209 offset:41184
	ds_read_b128 v[48:51], v211 offset:41184
	v_mfma_f32_32x32x16_f16 v[240:255], v[176:179], v[12:15], 0
	s_waitcnt lgkmcnt(3)
	v_mfma_f32_32x32x16_f16 v[88:103], v[160:163], v[188:191], v[88:103]
	v_mfma_f32_32x32x16_f16 v[240:255], v[172:175], v[188:191], v[240:255]
	v_mfma_f32_32x32x16_f16 v[88:103], v[168:171], v[184:187], v[88:103]
	v_mfma_f32_32x32x16_f16 v[240:255], v[164:167], v[184:187], v[240:255]
	ds_read_b128 v[52:55], v209 offset:44352
	ds_read_b128 v[184:187], v211 offset:44352
	s_waitcnt lgkmcnt(4)
	v_mfma_f32_32x32x16_f16 v[88:103], v[156:159], v[180:183], v[88:103]
	v_mfma_f32_32x32x16_f16 v[240:255], v[160:163], v[180:183], v[240:255]
	v_add_f32_e32 v84, v219, v84
	v_add_f32_e32 v85, v220, v85
	s_waitcnt lgkmcnt(3)
	v_mfma_f32_32x32x16_f16 v[240:255], v[168:171], v[40:43], v[240:255]
	v_add_f32_e32 v40, 0, v85
	v_max_f32_e32 v84, 0, v84
	v_max_f32_e32 v40, 0, v40
	v_cvt_pk_f16_f32 v43, v84, v40
	v_add_f32_e32 v7, v7, v82
	v_add_f32_e32 v40, v218, v83
	v_max_f32_e32 v7, 0, v7
	v_max_f32_e32 v40, 0, v40
	v_cvt_pk_f16_f32 v42, v7, v40
	v_add_f32_e32 v40, v203, v68
	v_add_f32_e32 v41, v204, v69
	v_max_f32_e32 v40, 0, v40
	v_max_f32_e32 v41, 0, v41
	s_waitcnt lgkmcnt(2)
	v_mfma_f32_32x32x16_f16 v[240:255], v[156:159], v[48:51], v[240:255]
	v_cvt_pk_f16_f32 v41, v40, v41
	v_add_f32_e32 v39, v39, v66
	v_add_f32_e32 v40, v202, v67
	v_max_f32_e32 v39, 0, v39
	v_max_f32_e32 v40, 0, v40
	ds_read_b128 v[180:183], v209 offset:45408
	ds_read_b128 v[188:191], v211 offset:45408
	v_add_f32_e32 v7, v221, v86
	v_cvt_pk_f16_f32 v40, v39, v40
	v_add_f32_e32 v39, v205, v70
	v_max_f32_e32 v7, 0, v7
	v_max_f32_e32 v39, 0, v39
	s_nop 1
	v_permlane32_swap_b32_e32 v39, v7
	v_permlane32_swap_b32_e32 v40, v42
	v_permlane32_swap_b32_e32 v41, v43
	v_lshl_add_u64 v[48:49], s[20:21], 0, v[194:195]
	v_cvt_pk_f16_f32 v7, v39, v7
	global_store_dwordx4 v[48:49], v[40:43], off offset:1024 sc1
	global_store_dword v[196:197], v7, off sc1
	s_waitcnt lgkmcnt(3)
	v_mfma_f32_32x32x16_f16 v[88:103], v[132:135], v[52:55], v[88:103]
	ds_read_b128 v[52:55], v209 offset:46464
	ds_read_b128 v[66:69], v211 offset:46464
	s_waitcnt lgkmcnt(4)
	v_mfma_f32_32x32x16_f16 v[88:103], v[140:143], v[184:187], v[88:103]
	s_waitcnt lgkmcnt(3)
	v_mfma_f32_32x32x16_f16 v[88:103], v[120:123], v[180:183], v[88:103]
	ds_read_b128 v[48:51], v209 offset:47520
	ds_read_b128 v[40:43], v211 offset:47520
	v_mfma_f32_32x32x16_f16 v[240:255], v[132:135], v[180:183], v[240:255]
	s_waitcnt lgkmcnt(4)
	v_mfma_f32_32x32x16_f16 v[88:103], v[152:155], v[188:191], v[88:103]
	v_mfma_f32_32x32x16_f16 v[240:255], v[140:143], v[188:191], v[240:255]
	s_waitcnt lgkmcnt(3)
	v_mfma_f32_32x32x16_f16 v[88:103], v[148:151], v[52:55], v[88:103]
	s_mov_b64 s[2:3], s[26:27]
	v_mfma_f32_32x32x16_f16 v[240:255], v[120:123], v[52:55], v[240:255]
	ds_read_b128 v[52:55], v209 offset:50688
	ds_read_b128 v[82:85], v211 offset:50688
	s_waitcnt vmcnt(3)
	ds_write_b128 v212, v[232:235] offset:16
	s_waitcnt vmcnt(2)
	ds_write_b32 v212, v230 offset:548
	s_waitcnt lgkmcnt(6)
	v_mfma_f32_32x32x16_f16 v[88:103], v[144:147], v[66:69], v[88:103]
	v_mfma_f32_32x32x16_f16 v[240:255], v[152:155], v[66:69], v[240:255]
	s_and_saveexec_b64 s[28:29], s[4:5]
	s_andn2_b64 s[2:3], s[26:27], exec
	s_and_b64 s[30:31], s[6:7], exec
	s_or_b64 s[2:3], s[2:3], s[30:31]
	ds_write_b32 v212, v230 offset:536
	s_or_b64 exec, exec, s[28:29]
	s_and_saveexec_b64 s[28:29], s[2:3]
	ds_write_b32 v212, v230 offset:560
	s_or_b64 exec, exec, s[28:29]
	s_waitcnt lgkmcnt(5)
	v_mfma_f32_32x32x16_f16 v[240:255], v[148:151], v[48:51], v[240:255]
	ds_read_b128 v[66:69], v209 offset:51744
	ds_read_b128 v[44:47], v211 offset:51744
	s_waitcnt lgkmcnt(6)
	v_mfma_f32_32x32x16_f16 v[240:255], v[144:147], v[40:43], v[240:255]
	s_waitcnt lgkmcnt(5)
	v_mfma_f32_32x32x16_f16 v[88:103], v[136:139], v[52:55], v[88:103]
	ds_read_b128 v[52:55], v209 offset:52800
	ds_read_b128 v[48:51], v211 offset:52800
	s_waitcnt lgkmcnt(6)
	v_mfma_f32_32x32x16_f16 v[88:103], v[108:111], v[82:85], v[88:103]
	s_and_saveexec_b64 s[2:3], s[0:1]
	s_cbranch_execz .LBB6_561
	s_mov_b64 s[30:31], s[26:27]
	ds_write_b128 v214, v[236:239] offset:16
	ds_write_b32 v214, v231 offset:548
	s_and_saveexec_b64 s[28:29], s[4:5]
	s_andn2_b64 s[30:31], s[26:27], exec
	s_and_b64 s[34:35], s[6:7], exec
	s_or_b64 s[30:31], s[30:31], s[34:35]
	ds_write_b32 v214, v231 offset:536
	s_or_b64 exec, exec, s[28:29]
	s_and_b64 exec, exec, s[30:31]
	ds_write_b32 v214, v231 offset:560
